# MoE epilogues: bias as one dword per lane fetched before the K-loop + row_newbcast DPP; epilogue vmcnt(0) drains replaced by counted waits
# speedup vs baseline: 1.0311x; 1.0035x over previous
.LBB0_1898:
	s_xor_b64 s[36:37], s[42:43], -1
	s_cmp_eq_u32 s88, 0
	s_cselect_b64 s[44:45], -1, 0
	s_and_b64 s[0:1], s[44:45], exec
	s_cselect_b32 s39, s58, s15
	s_cselect_b32 s38, s9, s14
	s_cselect_b32 s2, s59, s61
	s_cselect_b32 s3, s60, s62
	s_and_b64 s[0:1], s[42:43], exec
	s_cselect_b32 s90, s39, s17
	s_cselect_b32 s91, s38, s16
	s_ashr_i32 s35, s34, 31
	s_lshl_b64 s[0:1], s[34:35], 18
	s_add_u32 s40, s2, s0
	s_addc_u32 s41, s3, s1
	s_and_b64 s[0:1], s[42:43], exec
	s_cselect_b32 s35, s41, s19
	s_cselect_b32 s92, s40, s18
	s_cmp_eq_u32 s88, 1
	s_cselect_b64 s[46:47], -1, 0
	s_ashr_i32 s31, s30, 31
	s_lshl_b32 s2, s28, 4
	s_lshl_b64 s[0:1], s[30:31], 10
	s_ashr_i32 s3, s2, 31
	s_lshl_b32 s31, s30, 8
	v_lshl_add_u64 v[214:215], v[212:213], 0, s[0:1]
	s_lshl_b64 s[0:1], s[2:3], 2
	s_add_u32 s48, s56, s0
	s_mov_b32 s89, 0
	v_or_b32_e32 v245, s31, v217
	v_add_u32_e32 v246, s31, v216
	v_add_u32_e32 v247, s31, v236
	v_add_u32_e32 v248, s31, v237
	s_addc_u32 s49, s57, s1
	v_lshrrev_b32_e32 v19, 4, v0
	v_and_b32_e32 v19, 3, v19
	v_lshlrev_b32_e32 v19, 5, v19
	v_and_b32_e32 v1, 7, v0
	v_lshl_add_u32 v19, v1, 2, v19
	v_and_b32_e32 v1, 8, v0
	v_lshl_add_u32 v19, v1, 6, v19
	s_lshl_b32 s0, s7, 8
	s_ashr_i32 s1, s0, 31
	s_lshl_b64 s[0:1], s[0:1], 2
	s_cmp_lg_u32 s55, 0
	s_cbranch_scc1 .Lmoe_pf_down
	s_ashr_i32 s2, s10, 3
	s_ashr_i32 s3, s2, 31
	s_lshl_b64 s[2:3], s[2:3], 13
	s_add_u32 s2, s75, s2
	s_addc_u32 s3, s78, s3
	s_add_u32 s0, s2, s0
	s_addc_u32 s1, s3, s1
	s_lshl_b32 s2, s24, 2
	s_add_u32 s0, s0, s2
	s_addc_u32 s1, s1, 0
	s_branch .Lmoe_pf_go

.Lmoe_pf_go:
	global_load_dword v1, v19, s[0:1]

.LBB0_1939:
	s_nop 15
	s_nop 7
	s_cmp_lt_i32 s72, 0
	s_movk_i32 s90, 0xffef
	s_cbranch_scc1 .LBB0_1943
	s_waitcnt vmcnt(12)
	s_mov_b64 s[0:1], exec
	v_readlane_b32 s2, v255, 5
	v_readlane_b32 s3, v255, 6
	s_and_b64 s[2:3], s[0:1], s[2:3]
	s_mov_b64 exec, s[2:3]
	s_cbranch_execz .LBB0_1942
	s_lshl_b32 s72, s72, 4
	s_lshl_b64 s[2:3], s[72:73], 2
	s_add_u32 s2, s56, s2
	s_addc_u32 s3, s57, s3
	global_atomic_add v3, v219, s[2:3]

.LBB0_1943:
	v_mov_b32_e32 v4, v0
	s_lshl_b32 s0, s7, 8
	v_and_b32_e32 v5, 15, v4
	v_lshrrev_b32_e32 v4, 1, v4
	s_lshl_b32 s2, s8, 8
	s_ashr_i32 s1, s0, 31
	v_and_b32_e32 v28, 24, v4
	v_or_b32_e32 v4, s81, v5
	s_cmp_lg_u32 s55, 0
	v_mov_b32_e32 v29, v3
	v_lshlrev_b32_e32 v46, 2, v28
	v_add_u32_e32 v30, s2, v4
	s_cbranch_scc0 .LBB0_1949
	s_ashr_i32 s2, s10, 2
	s_ashr_i32 s3, s2, 31
	s_lshl_b64 s[2:3], s[2:3], 12
	s_add_u32 s31, s79, s2
	s_addc_u32 s33, s80, s3
	s_lshl_b64 s[2:3], s[0:1], 2
	s_add_u32 s2, s31, s2
	s_addc_u32 s3, s33, s3
	s_lshl_b32 s31, s24, 2
	s_add_u32 s2, s2, s31
	s_addc_u32 s3, s3, 0
	s_mov_b32 s44, 0x3e800000
	s_mov_b32 s46, 0x41800000
	v_mov_b32_e32 v42, v3
	v_mov_b32_e32 v43, v3
	v_ashrrev_i32_e32 v31, 31, v30
	v_lshlrev_b64 v[32:33], 10, v[30:31]
	v_lshl_add_u64 v[32:33], s[22:23], 0, v[32:33]
	v_lshl_add_u64 v[32:33], v[32:33], 0, s[0:1]
	v_lshl_add_u64 v[32:33], v[32:33], 0, s[24:25]
	v_lshl_add_u64 v[32:33], v[32:33], 0, v[28:29]
	v_mov_b32_e32 v44, v3
	v_mov_b32_e32 v45, v3
	s_mov_b64 s[2:3], 0x20000
	s_waitcnt vmcnt(12)
	v_mov_b32_dpp v20, v1 row_newbcast:4 row_mask:0xf bank_mask:0xf
	v_mov_b32_dpp v21, v1 row_newbcast:5 row_mask:0xf bank_mask:0xf
	v_mov_b32_dpp v22, v1 row_newbcast:6 row_mask:0xf bank_mask:0xf
	v_mov_b32_dpp v23, v1 row_newbcast:7 row_mask:0xf bank_mask:0xf
	v_mov_b32_dpp v24, v1 row_newbcast:0 row_mask:0xf bank_mask:0xf
	v_mov_b32_dpp v25, v1 row_newbcast:1 row_mask:0xf bank_mask:0xf
	v_mov_b32_dpp v26, v1 row_newbcast:2 row_mask:0xf bank_mask:0xf
	v_mov_b32_dpp v27, v1 row_newbcast:3 row_mask:0xf bank_mask:0xf
	v_mov_b32_dpp v4, v1 row_newbcast:12 row_mask:0xf bank_mask:0xf
	v_mov_b32_dpp v5, v1 row_newbcast:13 row_mask:0xf bank_mask:0xf
	v_mov_b32_dpp v6, v1 row_newbcast:14 row_mask:0xf bank_mask:0xf
	v_mov_b32_dpp v7, v1 row_newbcast:15 row_mask:0xf bank_mask:0xf
	v_mov_b32_dpp v8, v1 row_newbcast:8 row_mask:0xf bank_mask:0xf
	v_mov_b32_dpp v9, v1 row_newbcast:9 row_mask:0xf bank_mask:0xf
	v_mov_b32_dpp v10, v1 row_newbcast:10 row_mask:0xf bank_mask:0xf
	v_mov_b32_dpp v11, v1 row_newbcast:11 row_mask:0xf bank_mask:0xf
	v_pk_mul_f32 v[20:21], v[20:21], s[46:47] op_sel_hi:[1,0]
	v_pk_mul_f32 v[22:23], v[22:23], s[46:47] op_sel_hi:[1,0]
	v_pk_mul_f32 v[24:25], v[24:25], s[46:47] op_sel_hi:[1,0]
	v_pk_mul_f32 v[26:27], v[26:27], s[46:47] op_sel_hi:[1,0]
	v_pk_mul_f32 v[4:5], v[4:5], s[46:47] op_sel_hi:[1,0]
	v_pk_mul_f32 v[6:7], v[6:7], s[46:47] op_sel_hi:[1,0]
	v_pk_mul_f32 v[8:9], v[8:9], s[46:47] op_sel_hi:[1,0]
	v_pk_mul_f32 v[10:11], v[10:11], s[46:47] op_sel_hi:[1,0]
	v_pk_fma_f32 v[40:41], v[192:193], s[44:45], v[20:21] op_sel_hi:[1,0,1]
	v_pk_fma_f32 v[36:37], v[196:197], s[44:45], v[24:25] op_sel_hi:[1,0,1]
	v_cvt_pk_fp8_f32 v43, v40, v41
	v_cvt_pk_fp8_f32 v42, v36, v37
	v_pk_fma_f32 v[34:35], v[198:199], s[44:45], v[26:27] op_sel_hi:[1,0,1]
	v_pk_fma_f32 v[38:39], v[194:195], s[44:45], v[22:23] op_sel_hi:[1,0,1]
	v_cvt_pk_fp8_f32 v42, v34, v35 op_sel:[0,0,1]
	v_cvt_pk_fp8_f32 v43, v38, v39 op_sel:[0,0,1]
	v_pk_fma_f32 v[36:37], v[164:165], s[44:45], v[8:9] op_sel_hi:[1,0,1]
	v_pk_fma_f32 v[40:41], v[160:161], s[44:45], v[4:5] op_sel_hi:[1,0,1]
	global_store_dwordx2 v[32:33], v[42:43], off
	v_mov_b32_e32 v42, v3
	v_mov_b32_e32 v43, v3
	v_cvt_pk_fp8_f32 v42, v36, v37
	v_cvt_pk_fp8_f32 v43, v40, v41
	v_pk_fma_f32 v[34:35], v[166:167], s[44:45], v[10:11] op_sel_hi:[1,0,1]
	v_pk_fma_f32 v[38:39], v[162:163], s[44:45], v[6:7] op_sel_hi:[1,0,1]
	v_cvt_pk_fp8_f32 v42, v34, v35 op_sel:[0,0,1]
	v_cvt_pk_fp8_f32 v43, v38, v39 op_sel:[0,0,1]
	v_pk_fma_f32 v[38:39], v[188:189], s[44:45], v[24:25] op_sel_hi:[1,0,1]
	v_or_b32_e32 v34, 16, v30
	global_store_dwordx2 v[32:33], v[42:43], off offset:128
	v_pk_fma_f32 v[42:43], v[184:185], s[44:45], v[20:21] op_sel_hi:[1,0,1]
	v_cvt_pk_fp8_f32 v44, v38, v39
	v_ashrrev_i32_e32 v35, 31, v34
	v_cvt_pk_fp8_f32 v45, v42, v43
	v_pk_fma_f32 v[36:37], v[190:191], s[44:45], v[26:27] op_sel_hi:[1,0,1]
	v_pk_fma_f32 v[40:41], v[186:187], s[44:45], v[22:23] op_sel_hi:[1,0,1]
	v_lshlrev_b64 v[34:35], 10, v[34:35]
	v_lshl_add_u64 v[34:35], s[22:23], 0, v[34:35]
	v_cvt_pk_fp8_f32 v44, v36, v37 op_sel:[0,0,1]
	v_cvt_pk_fp8_f32 v45, v40, v41 op_sel:[0,0,1]
	v_lshl_add_u64 v[34:35], v[34:35], 0, s[0:1]
	v_lshl_add_u64 v[34:35], v[34:35], 0, s[24:25]
	v_lshl_add_u64 v[34:35], v[34:35], 0, v[28:29]
	v_pk_fma_f32 v[38:39], v[156:157], s[44:45], v[8:9] op_sel_hi:[1,0,1]
	v_pk_fma_f32 v[42:43], v[152:153], s[44:45], v[4:5] op_sel_hi:[1,0,1]
	global_store_dwordx2 v[34:35], v[44:45], off
	v_mov_b32_e32 v44, v3
	v_mov_b32_e32 v45, v3
	v_cvt_pk_fp8_f32 v44, v38, v39
	v_cvt_pk_fp8_f32 v45, v42, v43
	v_pk_fma_f32 v[36:37], v[158:159], s[44:45], v[10:11] op_sel_hi:[1,0,1]
	v_pk_fma_f32 v[40:41], v[154:155], s[44:45], v[6:7] op_sel_hi:[1,0,1]
	v_cvt_pk_fp8_f32 v44, v36, v37 op_sel:[0,0,1]
	v_cvt_pk_fp8_f32 v45, v40, v41 op_sel:[0,0,1]
	v_pk_fma_f32 v[38:39], v[180:181], s[44:45], v[24:25] op_sel_hi:[1,0,1]
	v_pk_fma_f32 v[36:37], v[182:183], s[44:45], v[26:27] op_sel_hi:[1,0,1]
	v_mov_b64_e32 v[42:43], v[38:39]
	v_pk_fma_f32 v[38:39], v[176:177], s[44:45], v[20:21] op_sel_hi:[1,0,1]
	global_store_dwordx2 v[34:35], v[44:45], off offset:128
	v_mov_b32_e32 v44, v3
	v_mov_b32_e32 v45, v3
	v_cvt_pk_fp8_f32 v44, v42, v43
	v_cvt_pk_fp8_f32 v45, v38, v39
	v_or_b32_e32 v34, 32, v30
	v_ashrrev_i32_e32 v35, 31, v34
	v_mov_b64_e32 v[40:41], v[36:37]
	v_pk_fma_f32 v[36:37], v[178:179], s[44:45], v[22:23] op_sel_hi:[1,0,1]
	v_lshlrev_b64 v[34:35], 10, v[34:35]
	v_lshl_add_u64 v[34:35], s[22:23], 0, v[34:35]
	v_cvt_pk_fp8_f32 v44, v40, v41 op_sel:[0,0,1]
	v_cvt_pk_fp8_f32 v45, v36, v37 op_sel:[0,0,1]
	v_lshl_add_u64 v[34:35], v[34:35], 0, s[0:1]
	v_lshl_add_u64 v[34:35], v[34:35], 0, s[24:25]
	v_lshl_add_u64 v[34:35], v[34:35], 0, v[28:29]
	v_pk_fma_f32 v[38:39], v[148:149], s[44:45], v[8:9] op_sel_hi:[1,0,1]
	v_pk_fma_f32 v[42:43], v[144:145], s[44:45], v[4:5] op_sel_hi:[1,0,1]
	global_store_dwordx2 v[34:35], v[44:45], off
	v_mov_b32_e32 v44, v3
	v_mov_b32_e32 v45, v3
	v_cvt_pk_fp8_f32 v44, v38, v39
	v_cvt_pk_fp8_f32 v45, v42, v43
	v_pk_fma_f32 v[36:37], v[150:151], s[44:45], v[10:11] op_sel_hi:[1,0,1]
	v_pk_fma_f32 v[40:41], v[146:147], s[44:45], v[6:7] op_sel_hi:[1,0,1]
	v_cvt_pk_fp8_f32 v44, v36, v37 op_sel:[0,0,1]
	v_cvt_pk_fp8_f32 v45, v40, v41 op_sel:[0,0,1]
	v_pk_fma_f32 v[38:39], v[172:173], s[44:45], v[24:25] op_sel_hi:[1,0,1]
	v_pk_fma_f32 v[42:43], v[168:169], s[44:45], v[20:21] op_sel_hi:[1,0,1]
	global_store_dwordx2 v[34:35], v[44:45], off offset:128
	v_mov_b32_e32 v44, v3
	v_mov_b32_e32 v45, v3
	v_cvt_pk_fp8_f32 v44, v38, v39
	v_cvt_pk_fp8_f32 v45, v42, v43
	v_or_b32_e32 v34, 48, v30
	v_ashrrev_i32_e32 v35, 31, v34
	v_pk_fma_f32 v[36:37], v[174:175], s[44:45], v[26:27] op_sel_hi:[1,0,1]
	v_pk_fma_f32 v[40:41], v[170:171], s[44:45], v[22:23] op_sel_hi:[1,0,1]
	v_lshlrev_b64 v[34:35], 10, v[34:35]
	v_lshl_add_u64 v[34:35], s[22:23], 0, v[34:35]
	v_cvt_pk_fp8_f32 v44, v36, v37 op_sel:[0,0,1]
	v_cvt_pk_fp8_f32 v45, v40, v41 op_sel:[0,0,1]
	v_lshl_add_u64 v[34:35], v[34:35], 0, s[0:1]
	v_lshl_add_u64 v[34:35], v[34:35], 0, s[24:25]
	v_lshl_add_u64 v[34:35], v[34:35], 0, v[28:29]
	v_pk_fma_f32 v[38:39], v[140:141], s[44:45], v[8:9] op_sel_hi:[1,0,1]
	v_pk_fma_f32 v[42:43], v[136:137], s[44:45], v[4:5] op_sel_hi:[1,0,1]
	global_store_dwordx2 v[34:35], v[44:45], off
	v_mov_b32_e32 v44, v3
	v_mov_b32_e32 v45, v3
	v_cvt_pk_fp8_f32 v44, v38, v39
	v_cvt_pk_fp8_f32 v45, v42, v43
	v_pk_fma_f32 v[36:37], v[142:143], s[44:45], v[10:11] op_sel_hi:[1,0,1]
	v_pk_fma_f32 v[40:41], v[138:139], s[44:45], v[6:7] op_sel_hi:[1,0,1]
	v_cvt_pk_fp8_f32 v44, v36, v37 op_sel:[0,0,1]
	v_cvt_pk_fp8_f32 v45, v40, v41 op_sel:[0,0,1]
	v_pk_fma_f32 v[38:39], v[132:133], s[44:45], v[24:25] op_sel_hi:[1,0,1]
	v_pk_fma_f32 v[42:43], v[128:129], s[44:45], v[20:21] op_sel_hi:[1,0,1]
	global_store_dwordx2 v[34:35], v[44:45], off offset:128
	v_mov_b32_e32 v44, v3
	v_mov_b32_e32 v45, v3
	v_cvt_pk_fp8_f32 v44, v38, v39
	v_cvt_pk_fp8_f32 v45, v42, v43
	v_pk_fma_f32 v[36:37], v[134:135], s[44:45], v[26:27] op_sel_hi:[1,0,1]
	v_pk_fma_f32 v[40:41], v[130:131], s[44:45], v[22:23] op_sel_hi:[1,0,1]
	v_cvt_pk_fp8_f32 v44, v36, v37 op_sel:[0,0,1]
	v_cvt_pk_fp8_f32 v45, v40, v41 op_sel:[0,0,1]
	v_lshl_add_u64 v[34:35], v[32:33], 0, s[2:3]
	s_mov_b32 s2, 0x20000
	v_add_co_u32_e32 v36, vcc, s2, v32
	v_pk_fma_f32 v[38:39], v[100:101], s[44:45], v[8:9] op_sel_hi:[1,0,1]
	s_nop 0
	v_addc_co_u32_e32 v37, vcc, 0, v33, vcc
	v_pk_fma_f32 v[42:43], v[96:97], s[44:45], v[4:5] op_sel_hi:[1,0,1]
	global_store_dwordx2 v[36:37], v[44:45], off
	v_mov_b32_e32 v44, v3
	v_mov_b32_e32 v45, v3
	v_cvt_pk_fp8_f32 v44, v38, v39
	v_cvt_pk_fp8_f32 v45, v42, v43
	v_pk_fma_f32 v[36:37], v[102:103], s[44:45], v[10:11] op_sel_hi:[1,0,1]
	v_pk_fma_f32 v[40:41], v[98:99], s[44:45], v[6:7] op_sel_hi:[1,0,1]
	v_cvt_pk_fp8_f32 v44, v36, v37 op_sel:[0,0,1]
	v_cvt_pk_fp8_f32 v45, v40, v41 op_sel:[0,0,1]
	v_pk_fma_f32 v[38:39], v[124:125], s[44:45], v[24:25] op_sel_hi:[1,0,1]
	v_pk_fma_f32 v[42:43], v[120:121], s[44:45], v[20:21] op_sel_hi:[1,0,1]
	global_store_dwordx2 v[34:35], v[44:45], off offset:128
	v_mov_b32_e32 v44, v3
	v_mov_b32_e32 v45, v3
	v_cvt_pk_fp8_f32 v44, v38, v39
	v_cvt_pk_fp8_f32 v45, v42, v43
	v_pk_fma_f32 v[36:37], v[126:127], s[44:45], v[26:27] op_sel_hi:[1,0,1]
	v_pk_fma_f32 v[40:41], v[122:123], s[44:45], v[22:23] op_sel_hi:[1,0,1]
	s_mov_b64 s[2:3], 0x24000
	v_cvt_pk_fp8_f32 v44, v36, v37 op_sel:[0,0,1]
	v_cvt_pk_fp8_f32 v45, v40, v41 op_sel:[0,0,1]
	v_lshl_add_u64 v[34:35], v[32:33], 0, s[2:3]
	s_mov_b32 s2, 0x24000
	v_add_co_u32_e32 v36, vcc, s2, v32
	v_pk_fma_f32 v[38:39], v[92:93], s[44:45], v[8:9] op_sel_hi:[1,0,1]
	s_nop 0
	v_addc_co_u32_e32 v37, vcc, 0, v33, vcc
	v_pk_fma_f32 v[42:43], v[88:89], s[44:45], v[4:5] op_sel_hi:[1,0,1]
	global_store_dwordx2 v[36:37], v[44:45], off
	v_mov_b32_e32 v44, v3
	v_mov_b32_e32 v45, v3
	v_cvt_pk_fp8_f32 v44, v38, v39
	v_cvt_pk_fp8_f32 v45, v42, v43
	v_pk_fma_f32 v[36:37], v[94:95], s[44:45], v[10:11] op_sel_hi:[1,0,1]
	v_pk_fma_f32 v[40:41], v[90:91], s[44:45], v[6:7] op_sel_hi:[1,0,1]
	v_cvt_pk_fp8_f32 v44, v36, v37 op_sel:[0,0,1]
	v_cvt_pk_fp8_f32 v45, v40, v41 op_sel:[0,0,1]
	v_pk_fma_f32 v[38:39], v[116:117], s[44:45], v[24:25] op_sel_hi:[1,0,1]
	v_pk_fma_f32 v[42:43], v[112:113], s[44:45], v[20:21] op_sel_hi:[1,0,1]
	global_store_dwordx2 v[34:35], v[44:45], off offset:128
	v_mov_b32_e32 v44, v3
	v_mov_b32_e32 v45, v3
	v_cvt_pk_fp8_f32 v44, v38, v39
	v_cvt_pk_fp8_f32 v45, v42, v43
	v_pk_fma_f32 v[36:37], v[118:119], s[44:45], v[26:27] op_sel_hi:[1,0,1]
	v_pk_fma_f32 v[40:41], v[114:115], s[44:45], v[22:23] op_sel_hi:[1,0,1]
	s_mov_b64 s[2:3], 0x28000
	v_cvt_pk_fp8_f32 v44, v36, v37 op_sel:[0,0,1]
	v_cvt_pk_fp8_f32 v45, v40, v41 op_sel:[0,0,1]
	v_lshl_add_u64 v[34:35], v[32:33], 0, s[2:3]
	s_mov_b32 s2, 0x28000
	v_add_co_u32_e32 v36, vcc, s2, v32
	v_pk_fma_f32 v[38:39], v[84:85], s[44:45], v[8:9] op_sel_hi:[1,0,1]
	s_nop 0
	v_addc_co_u32_e32 v37, vcc, 0, v33, vcc
	global_store_dwordx2 v[36:37], v[44:45], off
	v_mov_b32_e32 v44, v3
	v_pk_fma_f32 v[42:43], v[80:81], s[44:45], v[4:5] op_sel_hi:[1,0,1]
	v_cvt_pk_fp8_f32 v44, v38, v39
	v_mov_b32_e32 v45, v3
	v_pk_fma_f32 v[36:37], v[86:87], s[44:45], v[10:11] op_sel_hi:[1,0,1]
	v_cvt_pk_fp8_f32 v45, v42, v43
	v_pk_fma_f32 v[24:25], v[108:109], s[44:45], v[24:25] op_sel_hi:[1,0,1]
	v_pk_fma_f32 v[20:21], v[104:105], s[44:45], v[20:21] op_sel_hi:[1,0,1]
	v_pk_fma_f32 v[40:41], v[82:83], s[44:45], v[6:7] op_sel_hi:[1,0,1]
	v_cvt_pk_fp8_f32 v44, v36, v37 op_sel:[0,0,1]
	v_mov_b32_e32 v36, v3
	v_mov_b32_e32 v37, v3
	v_cvt_pk_fp8_f32 v36, v24, v25
	v_cvt_pk_fp8_f32 v37, v20, v21
	v_cvt_pk_fp8_f32 v45, v40, v41 op_sel:[0,0,1]
	v_pk_fma_f32 v[26:27], v[110:111], s[44:45], v[26:27] op_sel_hi:[1,0,1]
	v_pk_fma_f32 v[22:23], v[106:107], s[44:45], v[22:23] op_sel_hi:[1,0,1]
	s_mov_b64 s[2:3], 0x2c000
	v_cvt_pk_fp8_f32 v36, v26, v27 op_sel:[0,0,1]
	v_cvt_pk_fp8_f32 v37, v22, v23 op_sel:[0,0,1]
	global_store_dwordx2 v[34:35], v[44:45], off offset:128
	v_lshl_add_u64 v[34:35], v[32:33], 0, s[2:3]
	s_mov_b32 s2, 0x2c000
	v_add_co_u32_e32 v20, vcc, s2, v32
	v_pk_fma_f32 v[8:9], v[76:77], s[44:45], v[8:9] op_sel_hi:[1,0,1]
	s_nop 0
	v_addc_co_u32_e32 v21, vcc, 0, v33, vcc
	v_pk_fma_f32 v[4:5], v[12:13], s[44:45], v[4:5] op_sel_hi:[1,0,1]
	global_store_dwordx2 v[20:21], v[36:37], off
	v_mov_b32_e32 v20, v3
	v_mov_b32_e32 v21, v3
	v_cvt_pk_fp8_f32 v20, v8, v9
	v_cvt_pk_fp8_f32 v21, v4, v5
	v_pk_fma_f32 v[10:11], v[78:79], s[44:45], v[10:11] op_sel_hi:[1,0,1]
	v_pk_fma_f32 v[6:7], v[14:15], s[44:45], v[6:7] op_sel_hi:[1,0,1]
	v_cvt_pk_fp8_f32 v20, v10, v11 op_sel:[0,0,1]
	v_cvt_pk_fp8_f32 v21, v6, v7 op_sel:[0,0,1]
	global_store_dwordx2 v[34:35], v[20:21], off offset:128
	s_cbranch_execnz .LBB0_1946
.LBB0_1945:
	s_ashr_i32 s2, s10, 3
	s_ashr_i32 s3, s2, 31
	s_lshl_b64 s[2:3], s[2:3], 13
	s_add_u32 s2, s75, s2
	s_addc_u32 s3, s78, s3
	s_lshl_b64 s[0:1], s[0:1], 2
	s_add_u32 s0, s2, s0
	s_addc_u32 s1, s3, s1
	s_lshl_b32 s2, s24, 2
	s_add_u32 s0, s0, s2
	s_addc_u32 s1, s1, 0
	v_ashrrev_i32_e32 v31, 31, v30
	s_mov_b32 s2, 0xc0c00000
	s_lshl_b32 s0, s7, 7
	s_ashr_i32 s1, s0, 31
	s_mov_b32 s72, s6
	s_waitcnt vmcnt(12)
	v_mov_b32_dpp v4, v1 row_newbcast:4 row_mask:0xf bank_mask:0xf
	v_mov_b32_dpp v5, v1 row_newbcast:5 row_mask:0xf bank_mask:0xf
	v_mov_b32_dpp v6, v1 row_newbcast:6 row_mask:0xf bank_mask:0xf
	v_mov_b32_dpp v7, v1 row_newbcast:7 row_mask:0xf bank_mask:0xf
	v_mov_b32_dpp v8, v1 row_newbcast:0 row_mask:0xf bank_mask:0xf
	v_mov_b32_dpp v9, v1 row_newbcast:1 row_mask:0xf bank_mask:0xf
	v_mov_b32_dpp v10, v1 row_newbcast:2 row_mask:0xf bank_mask:0xf
	v_mov_b32_dpp v11, v1 row_newbcast:3 row_mask:0xf bank_mask:0xf
	v_mov_b32_dpp v22, v1 row_newbcast:12 row_mask:0xf bank_mask:0xf
	v_mov_b32_dpp v23, v1 row_newbcast:13 row_mask:0xf bank_mask:0xf
	v_mov_b32_dpp v24, v1 row_newbcast:14 row_mask:0xf bank_mask:0xf
	v_mov_b32_dpp v25, v1 row_newbcast:15 row_mask:0xf bank_mask:0xf
	v_mov_b32_dpp v32, v1 row_newbcast:8 row_mask:0xf bank_mask:0xf
	v_mov_b32_dpp v33, v1 row_newbcast:9 row_mask:0xf bank_mask:0xf
	v_mov_b32_dpp v34, v1 row_newbcast:10 row_mask:0xf bank_mask:0xf
	v_mov_b32_dpp v35, v1 row_newbcast:11 row_mask:0xf bank_mask:0xf
	v_pk_add_f32 v[20:21], v[24:25], 1.0 op_sel_hi:[1,0]
	v_lshlrev_b64 v[24:25], 10, v[30:31]
	v_fmamk_f32 v31, v196, 0x3c800000, v8
	v_min_f32_e32 v31, 0x40e00000, v31
	v_pk_add_f32 v[26:27], v[34:35], 1.0 op_sel_hi:[1,0]
	v_mul_f32_e32 v35, 0xc01d265f, v31
	v_exp_f32_e32 v35, v35
	v_pk_add_f32 v[32:33], v[32:33], 1.0 op_sel_hi:[1,0]
	v_pk_add_f32 v[22:23], v[22:23], 1.0 op_sel_hi:[1,0]
	v_fmamk_f32 v34, v164, 0x3c800000, v32
	v_add_f32_e32 v35, 1.0, v35
	v_rcp_f32_e32 v35, v35
	v_med3_f32 v34, v34, s2, v250
	v_lshl_add_u64 v[24:25], s[14:15], 0, v[24:25]
	v_lshl_add_u64 v[24:25], v[24:25], 0, s[0:1]
	v_mul_f32_e32 v31, v31, v35
	v_mul_f32_e32 v31, v34, v31
	v_fmamk_f32 v34, v197, 0x3c800000, v9
	v_min_f32_e32 v34, 0x40e00000, v34
	v_mul_f32_e32 v36, 0xc01d265f, v34
	v_exp_f32_e32 v36, v36
	v_fmamk_f32 v35, v165, 0x3c800000, v33
	v_med3_f32 v35, v35, s2, v250
	v_lshl_add_u64 v[24:25], v[24:25], 0, s[24:25]
	v_add_f32_e32 v36, 1.0, v36
	v_rcp_f32_e32 v36, v36
	v_lshl_add_u64 v[24:25], v[24:25], 0, v[28:29]
	v_mul_f32_e32 v34, v34, v36
	v_mul_f32_e32 v35, v35, v34
	v_fmamk_f32 v34, v198, 0x3c800000, v10
	v_min_f32_e32 v34, 0x40e00000, v34
	v_mul_f32_e32 v37, 0xc01d265f, v34
	v_exp_f32_e32 v37, v37
	v_fmamk_f32 v36, v166, 0x3c800000, v26
	v_med3_f32 v36, v36, s2, v250
	v_add_f32_e32 v37, 1.0, v37
	v_rcp_f32_e32 v37, v37
	s_nop 0
	v_mul_f32_e32 v34, v34, v37
	v_mul_f32_e32 v36, v36, v34
	v_fmamk_f32 v34, v199, 0x3c800000, v11
	v_min_f32_e32 v34, 0x40e00000, v34
	v_mul_f32_e32 v38, 0xc01d265f, v34
	v_exp_f32_e32 v38, v38
	v_fmamk_f32 v37, v167, 0x3c800000, v27
	v_med3_f32 v37, v37, s2, v250
	v_add_f32_e32 v38, 1.0, v38
	v_rcp_f32_e32 v38, v38
	s_nop 0
	v_mul_f32_e32 v34, v34, v38
	v_mul_f32_e32 v37, v37, v34
	v_fmamk_f32 v34, v192, 0x3c800000, v4
	v_min_f32_e32 v34, 0x40e00000, v34
	v_mul_f32_e32 v39, 0xc01d265f, v34
	v_exp_f32_e32 v39, v39
	v_fmamk_f32 v38, v160, 0x3c800000, v22
	v_med3_f32 v38, v38, s2, v250
	v_add_f32_e32 v39, 1.0, v39
	v_rcp_f32_e32 v39, v39
	s_nop 0
	v_mul_f32_e32 v34, v34, v39
	v_mul_f32_e32 v38, v38, v34
	v_fmamk_f32 v34, v193, 0x3c800000, v5
	v_min_f32_e32 v34, 0x40e00000, v34
	v_mul_f32_e32 v40, 0xc01d265f, v34
	v_exp_f32_e32 v40, v40
	v_fmamk_f32 v39, v161, 0x3c800000, v23
	v_med3_f32 v39, v39, s2, v250
	v_add_f32_e32 v40, 1.0, v40
	v_rcp_f32_e32 v40, v40
	s_nop 0
	v_mul_f32_e32 v34, v34, v40
	v_mul_f32_e32 v40, v39, v34
	v_fmamk_f32 v34, v194, 0x3c800000, v6
	v_min_f32_e32 v34, 0x40e00000, v34
	v_mul_f32_e32 v41, 0xc01d265f, v34
	v_exp_f32_e32 v41, v41
	v_fmamk_f32 v39, v162, 0x3c800000, v20
	v_med3_f32 v39, v39, s2, v250
	v_add_f32_e32 v41, 1.0, v41
	v_rcp_f32_e32 v41, v41
	s_nop 0
	v_mul_f32_e32 v34, v34, v41
	v_mul_f32_e32 v39, v39, v34
	v_fmamk_f32 v34, v195, 0x3c800000, v7
	v_min_f32_e32 v34, 0x40e00000, v34
	v_mul_f32_e32 v42, 0xc01d265f, v34
	v_exp_f32_e32 v42, v42
	v_fmamk_f32 v41, v163, 0x3c800000, v21
	v_med3_f32 v41, v41, s2, v250
	v_add_f32_e32 v42, 1.0, v42
	v_rcp_f32_e32 v42, v42
	s_nop 0
	v_mul_f32_e32 v34, v34, v42
	v_mul_f32_e32 v41, v41, v34
	v_mov_b32_e32 v34, v3
	v_cvt_pk_fp8_f32 v34, v31, v35
	v_fmamk_f32 v31, v188, 0x3c800000, v8
	v_min_f32_e32 v31, 0x40e00000, v31
	v_mov_b32_e32 v35, v3
	v_cvt_pk_fp8_f32 v34, v36, v37 op_sel:[0,0,1]
	v_mul_f32_e32 v37, 0xc01d265f, v31
	v_exp_f32_e32 v37, v37
	v_fmamk_f32 v36, v156, 0x3c800000, v32
	v_med3_f32 v36, v36, s2, v250
	v_cvt_pk_fp8_f32 v35, v38, v40
	v_add_f32_e32 v37, 1.0, v37
	v_rcp_f32_e32 v37, v37
	v_cvt_pk_fp8_f32 v35, v39, v41 op_sel:[0,0,1]
	s_nop 0
	global_store_dwordx2 v[24:25], v[34:35], off sc1
	v_mul_f32_e32 v31, v31, v37
	v_mul_f32_e32 v31, v36, v31
	v_fmamk_f32 v36, v189, 0x3c800000, v9
	v_min_f32_e32 v36, 0x40e00000, v36
	v_mul_f32_e32 v38, 0xc01d265f, v36
	v_exp_f32_e32 v38, v38
	v_fmamk_f32 v37, v157, 0x3c800000, v33
	v_med3_f32 v37, v37, s2, v250
	v_or_b32_e32 v34, 16, v30
	v_add_f32_e32 v38, 1.0, v38
	v_rcp_f32_e32 v38, v38
	v_ashrrev_i32_e32 v35, 31, v34
	v_lshlrev_b64 v[34:35], 10, v[34:35]
	v_lshl_add_u64 v[34:35], s[14:15], 0, v[34:35]
	v_mul_f32_e32 v36, v36, v38
	v_mul_f32_e32 v37, v37, v36
	v_fmamk_f32 v36, v190, 0x3c800000, v10
	v_min_f32_e32 v36, 0x40e00000, v36
	v_mul_f32_e32 v39, 0xc01d265f, v36
	v_exp_f32_e32 v39, v39
	v_fmamk_f32 v38, v158, 0x3c800000, v26
	v_med3_f32 v38, v38, s2, v250
	v_lshl_add_u64 v[34:35], v[34:35], 0, s[0:1]
	v_add_f32_e32 v39, 1.0, v39
	v_rcp_f32_e32 v39, v39
	v_lshl_add_u64 v[34:35], v[34:35], 0, s[24:25]
	v_lshl_add_u64 v[34:35], v[34:35], 0, v[28:29]
	v_mul_f32_e32 v36, v36, v39
	v_mul_f32_e32 v38, v38, v36
	v_fmamk_f32 v36, v191, 0x3c800000, v11
	v_min_f32_e32 v36, 0x40e00000, v36
	v_mul_f32_e32 v40, 0xc01d265f, v36
	v_exp_f32_e32 v40, v40
	v_fmamk_f32 v39, v159, 0x3c800000, v27
	v_med3_f32 v39, v39, s2, v250
	v_add_f32_e32 v40, 1.0, v40
	v_rcp_f32_e32 v40, v40
	s_nop 0
	v_mul_f32_e32 v36, v36, v40
	v_mul_f32_e32 v39, v39, v36
	v_fmamk_f32 v36, v184, 0x3c800000, v4
	v_min_f32_e32 v36, 0x40e00000, v36
	v_mul_f32_e32 v41, 0xc01d265f, v36
	v_exp_f32_e32 v41, v41
	v_fmamk_f32 v40, v152, 0x3c800000, v22
	v_med3_f32 v40, v40, s2, v250
	v_add_f32_e32 v41, 1.0, v41
	v_rcp_f32_e32 v41, v41
	s_nop 0
	v_mul_f32_e32 v36, v36, v41
	v_mul_f32_e32 v40, v40, v36
	v_fmamk_f32 v36, v185, 0x3c800000, v5
	v_min_f32_e32 v36, 0x40e00000, v36
	v_mul_f32_e32 v42, 0xc01d265f, v36
	v_exp_f32_e32 v42, v42
	v_fmamk_f32 v41, v153, 0x3c800000, v23
	v_med3_f32 v41, v41, s2, v250
	v_add_f32_e32 v42, 1.0, v42
	v_rcp_f32_e32 v42, v42
	s_nop 0
	v_mul_f32_e32 v36, v36, v42
	v_mul_f32_e32 v41, v41, v36
	v_fmamk_f32 v36, v186, 0x3c800000, v6
	v_min_f32_e32 v36, 0x40e00000, v36
	v_mul_f32_e32 v43, 0xc01d265f, v36
	v_exp_f32_e32 v43, v43
	v_fmamk_f32 v42, v154, 0x3c800000, v20
	v_med3_f32 v42, v42, s2, v250
	v_add_f32_e32 v43, 1.0, v43
	v_rcp_f32_e32 v43, v43
	s_nop 0
	v_mul_f32_e32 v36, v36, v43
	v_mul_f32_e32 v42, v42, v36
	v_fmamk_f32 v36, v187, 0x3c800000, v7
	v_min_f32_e32 v36, 0x40e00000, v36
	v_mul_f32_e32 v44, 0xc01d265f, v36
	v_exp_f32_e32 v44, v44
	v_fmamk_f32 v43, v155, 0x3c800000, v21
	v_med3_f32 v43, v43, s2, v250
	v_add_f32_e32 v44, 1.0, v44
	v_rcp_f32_e32 v44, v44
	s_nop 0
	v_mul_f32_e32 v36, v36, v44
	v_mul_f32_e32 v43, v43, v36
	v_mov_b32_e32 v36, v3
	v_cvt_pk_fp8_f32 v36, v31, v37
	v_mov_b32_e32 v37, v3
	v_cvt_pk_fp8_f32 v37, v40, v41
	v_fmamk_f32 v31, v180, 0x3c800000, v8
	v_min_f32_e32 v31, 0x40e00000, v31
	v_cvt_pk_fp8_f32 v36, v38, v39 op_sel:[0,0,1]
	v_cvt_pk_fp8_f32 v37, v42, v43 op_sel:[0,0,1]
	s_nop 0
	global_store_dwordx2 v[34:35], v[36:37], off sc1
	v_mul_f32_e32 v37, 0xc01d265f, v31
	v_exp_f32_e32 v37, v37
	v_fmamk_f32 v36, v148, 0x3c800000, v32
	v_med3_f32 v36, v36, s2, v250
	v_or_b32_e32 v34, 32, v30
	v_add_f32_e32 v37, 1.0, v37
	v_rcp_f32_e32 v37, v37
	v_ashrrev_i32_e32 v35, 31, v34
	v_lshlrev_b64 v[34:35], 10, v[34:35]
	v_lshl_add_u64 v[34:35], s[14:15], 0, v[34:35]
	v_mul_f32_e32 v31, v31, v37
	v_mul_f32_e32 v31, v36, v31
	v_fmamk_f32 v36, v181, 0x3c800000, v9
	v_min_f32_e32 v36, 0x40e00000, v36
	v_mul_f32_e32 v38, 0xc01d265f, v36
	v_exp_f32_e32 v38, v38
	v_fmamk_f32 v37, v149, 0x3c800000, v33
	v_med3_f32 v37, v37, s2, v250
	v_lshl_add_u64 v[34:35], v[34:35], 0, s[0:1]
	v_add_f32_e32 v38, 1.0, v38
	v_rcp_f32_e32 v38, v38
	v_lshl_add_u64 v[34:35], v[34:35], 0, s[24:25]
	v_lshl_add_u64 v[34:35], v[34:35], 0, v[28:29]
	v_or_b32_e32 v30, 48, v30
	v_mul_f32_e32 v36, v36, v38
	v_mul_f32_e32 v37, v37, v36
	v_fmamk_f32 v36, v182, 0x3c800000, v10
	v_min_f32_e32 v36, 0x40e00000, v36
	v_mul_f32_e32 v39, 0xc01d265f, v36
	v_exp_f32_e32 v39, v39
	v_fmamk_f32 v38, v150, 0x3c800000, v26
	v_med3_f32 v38, v38, s2, v250
	v_add_f32_e32 v39, 1.0, v39
	v_rcp_f32_e32 v39, v39
	s_nop 0
	v_mul_f32_e32 v36, v36, v39
	v_mul_f32_e32 v38, v38, v36
	v_fmamk_f32 v36, v183, 0x3c800000, v11
	v_min_f32_e32 v36, 0x40e00000, v36
	v_mul_f32_e32 v40, 0xc01d265f, v36
	v_exp_f32_e32 v40, v40
	v_fmamk_f32 v39, v151, 0x3c800000, v27
	v_med3_f32 v39, v39, s2, v250
	v_add_f32_e32 v40, 1.0, v40
	v_rcp_f32_e32 v40, v40
	s_nop 0
	v_mul_f32_e32 v36, v36, v40
	v_mul_f32_e32 v39, v39, v36
	v_fmamk_f32 v36, v176, 0x3c800000, v4
	v_min_f32_e32 v36, 0x40e00000, v36
	v_mul_f32_e32 v41, 0xc01d265f, v36
	v_exp_f32_e32 v41, v41
	v_fmamk_f32 v40, v144, 0x3c800000, v22
	v_med3_f32 v40, v40, s2, v250
	v_add_f32_e32 v41, 1.0, v41
	v_rcp_f32_e32 v41, v41
	s_nop 0
	v_mul_f32_e32 v36, v36, v41
	v_mul_f32_e32 v40, v40, v36
	v_fmamk_f32 v36, v177, 0x3c800000, v5
	v_min_f32_e32 v36, 0x40e00000, v36
	v_mul_f32_e32 v42, 0xc01d265f, v36
	v_exp_f32_e32 v42, v42
	v_fmamk_f32 v41, v145, 0x3c800000, v23
	v_med3_f32 v41, v41, s2, v250
	v_add_f32_e32 v42, 1.0, v42
	v_rcp_f32_e32 v42, v42
	s_nop 0
	v_mul_f32_e32 v36, v36, v42
	v_mul_f32_e32 v41, v41, v36
	v_fmamk_f32 v36, v178, 0x3c800000, v6
	v_min_f32_e32 v36, 0x40e00000, v36
	v_mul_f32_e32 v43, 0xc01d265f, v36
	v_exp_f32_e32 v43, v43
	v_fmamk_f32 v42, v146, 0x3c800000, v20
	v_med3_f32 v42, v42, s2, v250
	v_add_f32_e32 v43, 1.0, v43
	v_rcp_f32_e32 v43, v43
	s_nop 0
	v_mul_f32_e32 v36, v36, v43
	v_mul_f32_e32 v42, v42, v36
	v_fmamk_f32 v36, v179, 0x3c800000, v7
	v_min_f32_e32 v36, 0x40e00000, v36
	v_mul_f32_e32 v44, 0xc01d265f, v36
	v_exp_f32_e32 v44, v44
	v_fmamk_f32 v43, v147, 0x3c800000, v21
	v_med3_f32 v43, v43, s2, v250
	v_add_f32_e32 v44, 1.0, v44
	v_rcp_f32_e32 v44, v44
	s_nop 0
	v_mul_f32_e32 v36, v36, v44
	v_mul_f32_e32 v43, v43, v36
	v_mov_b32_e32 v36, v3
	v_cvt_pk_fp8_f32 v36, v31, v37
	v_mov_b32_e32 v37, v3
	v_cvt_pk_fp8_f32 v37, v40, v41
	v_ashrrev_i32_e32 v31, 31, v30
	v_cvt_pk_fp8_f32 v36, v38, v39 op_sel:[0,0,1]
	v_lshlrev_b64 v[30:31], 10, v[30:31]
	v_cvt_pk_fp8_f32 v37, v42, v43 op_sel:[0,0,1]
	v_lshl_add_u64 v[30:31], s[14:15], 0, v[30:31]
	global_store_dwordx2 v[34:35], v[36:37], off sc1
	v_fmamk_f32 v34, v172, 0x3c800000, v8
	v_min_f32_e32 v34, 0x40e00000, v34
	v_mul_f32_e32 v36, 0xc01d265f, v34
	v_exp_f32_e32 v36, v36
	v_fmamk_f32 v35, v140, 0x3c800000, v32
	v_med3_f32 v35, v35, s2, v250
	v_lshl_add_u64 v[30:31], v[30:31], 0, s[0:1]
	v_add_f32_e32 v36, 1.0, v36
	v_rcp_f32_e32 v36, v36
	v_lshl_add_u64 v[30:31], v[30:31], 0, s[24:25]
	v_lshl_add_u64 v[28:29], v[30:31], 0, v[28:29]
	v_mov_b32_e32 v30, v3
	v_mul_f32_e32 v34, v34, v36
	v_mul_f32_e32 v34, v35, v34
	v_fmamk_f32 v35, v173, 0x3c800000, v9
	v_min_f32_e32 v35, 0x40e00000, v35
	v_mul_f32_e32 v37, 0xc01d265f, v35
	v_exp_f32_e32 v37, v37
	v_fmamk_f32 v36, v141, 0x3c800000, v33
	v_med3_f32 v36, v36, s2, v250
	v_mov_b32_e32 v31, v3
	v_add_f32_e32 v37, 1.0, v37
	v_rcp_f32_e32 v37, v37
	s_mov_b64 s[0:1], 0x20000
	v_mul_f32_e32 v35, v35, v37
	v_mul_f32_e32 v35, v36, v35
	v_fmamk_f32 v36, v174, 0x3c800000, v10
	v_min_f32_e32 v36, 0x40e00000, v36
	v_mul_f32_e32 v38, 0xc01d265f, v36
	v_exp_f32_e32 v38, v38
	v_fmamk_f32 v37, v142, 0x3c800000, v26
	v_med3_f32 v37, v37, s2, v250
	v_cvt_pk_fp8_f32 v30, v34, v35
	v_add_f32_e32 v38, 1.0, v38
	v_rcp_f32_e32 v38, v38
	s_nop 0
	v_mul_f32_e32 v36, v36, v38
	v_mul_f32_e32 v36, v37, v36
	v_fmamk_f32 v37, v175, 0x3c800000, v11
	v_min_f32_e32 v37, 0x40e00000, v37
	v_mul_f32_e32 v39, 0xc01d265f, v37
	v_exp_f32_e32 v39, v39
	v_fmamk_f32 v38, v143, 0x3c800000, v27
	v_med3_f32 v38, v38, s2, v250
	v_add_f32_e32 v39, 1.0, v39
	v_rcp_f32_e32 v39, v39
	s_nop 0
	v_mul_f32_e32 v37, v37, v39
	v_mul_f32_e32 v37, v38, v37
	v_fmamk_f32 v38, v168, 0x3c800000, v4
	v_min_f32_e32 v38, 0x40e00000, v38
	v_mul_f32_e32 v40, 0xc01d265f, v38
	v_exp_f32_e32 v40, v40
	v_fmamk_f32 v39, v136, 0x3c800000, v22
	v_med3_f32 v39, v39, s2, v250
	v_cvt_pk_fp8_f32 v30, v36, v37 op_sel:[0,0,1]
	v_add_f32_e32 v40, 1.0, v40
	v_rcp_f32_e32 v40, v40
	s_nop 0
	v_mul_f32_e32 v38, v38, v40
	v_mul_f32_e32 v38, v39, v38
	v_fmamk_f32 v39, v169, 0x3c800000, v5
	v_min_f32_e32 v39, 0x40e00000, v39
	v_mul_f32_e32 v41, 0xc01d265f, v39
	v_exp_f32_e32 v41, v41
	v_fmamk_f32 v40, v137, 0x3c800000, v23
	v_med3_f32 v40, v40, s2, v250
	v_add_f32_e32 v41, 1.0, v41
	v_rcp_f32_e32 v41, v41
	s_nop 0
	v_mul_f32_e32 v39, v39, v41
	v_mul_f32_e32 v39, v40, v39
	v_fmamk_f32 v40, v170, 0x3c800000, v6
	v_min_f32_e32 v40, 0x40e00000, v40
	v_mul_f32_e32 v42, 0xc01d265f, v40
	v_exp_f32_e32 v42, v42
	v_fmamk_f32 v41, v138, 0x3c800000, v20
	v_med3_f32 v41, v41, s2, v250
	v_cvt_pk_fp8_f32 v31, v38, v39
	v_add_f32_e32 v42, 1.0, v42
	v_rcp_f32_e32 v42, v42
	s_nop 0
	v_mul_f32_e32 v40, v40, v42
	v_mul_f32_e32 v40, v41, v40
	v_fmamk_f32 v41, v171, 0x3c800000, v7
	v_min_f32_e32 v41, 0x40e00000, v41
	v_mul_f32_e32 v43, 0xc01d265f, v41
	v_exp_f32_e32 v43, v43
	v_fmamk_f32 v42, v139, 0x3c800000, v21
	v_med3_f32 v42, v42, s2, v250
	v_add_f32_e32 v43, 1.0, v43
	v_rcp_f32_e32 v43, v43
	s_nop 0
	v_mul_f32_e32 v41, v41, v43
	v_mul_f32_e32 v41, v42, v41
	v_cvt_pk_fp8_f32 v31, v40, v41 op_sel:[0,0,1]
	s_nop 0
	global_store_dwordx2 v[28:29], v[30:31], off sc1
	v_fmamk_f32 v28, v132, 0x3c800000, v8
	v_min_f32_e32 v28, 0x40e00000, v28
	v_mul_f32_e32 v30, 0xc01d265f, v28
	v_exp_f32_e32 v30, v30
	v_fmamk_f32 v29, v100, 0x3c800000, v32
	v_med3_f32 v29, v29, s2, v250
	v_add_f32_e32 v30, 1.0, v30
	v_rcp_f32_e32 v30, v30
	s_nop 0
	v_mul_f32_e32 v28, v28, v30
	v_mul_f32_e32 v31, v29, v28
	v_fmamk_f32 v28, v133, 0x3c800000, v9
	v_min_f32_e32 v28, 0x40e00000, v28
	v_mul_f32_e32 v30, 0xc01d265f, v28
	v_exp_f32_e32 v30, v30
	v_fmamk_f32 v29, v101, 0x3c800000, v33
	v_med3_f32 v29, v29, s2, v250
	v_add_f32_e32 v30, 1.0, v30
	v_rcp_f32_e32 v30, v30
	s_nop 0
	v_mul_f32_e32 v28, v28, v30
	v_mul_f32_e32 v34, v29, v28
	v_fmamk_f32 v28, v134, 0x3c800000, v10
	v_min_f32_e32 v28, 0x40e00000, v28
	v_mul_f32_e32 v30, 0xc01d265f, v28
	v_exp_f32_e32 v30, v30
	v_fmamk_f32 v29, v102, 0x3c800000, v26
	v_med3_f32 v29, v29, s2, v250
	v_add_f32_e32 v30, 1.0, v30
	v_rcp_f32_e32 v30, v30
	s_nop 0
	v_mul_f32_e32 v28, v28, v30
	v_mul_f32_e32 v35, v29, v28
	v_fmamk_f32 v28, v135, 0x3c800000, v11
	v_min_f32_e32 v28, 0x40e00000, v28
	v_mul_f32_e32 v30, 0xc01d265f, v28
	v_exp_f32_e32 v30, v30
	v_fmamk_f32 v29, v103, 0x3c800000, v27
	v_med3_f32 v29, v29, s2, v250
	v_add_f32_e32 v30, 1.0, v30
	v_rcp_f32_e32 v30, v30
	s_nop 0
	v_mul_f32_e32 v28, v28, v30
	v_mul_f32_e32 v36, v29, v28
	v_fmamk_f32 v28, v128, 0x3c800000, v4
	v_min_f32_e32 v28, 0x40e00000, v28
	v_mul_f32_e32 v30, 0xc01d265f, v28
	v_exp_f32_e32 v30, v30
	v_fmamk_f32 v29, v96, 0x3c800000, v22
	v_med3_f32 v29, v29, s2, v250
	v_add_f32_e32 v30, 1.0, v30
	v_rcp_f32_e32 v30, v30
	s_nop 0
	v_mul_f32_e32 v28, v28, v30
	v_mul_f32_e32 v37, v29, v28
	v_fmamk_f32 v28, v129, 0x3c800000, v5
	v_min_f32_e32 v28, 0x40e00000, v28
	v_mul_f32_e32 v30, 0xc01d265f, v28
	v_exp_f32_e32 v30, v30
	v_fmamk_f32 v29, v97, 0x3c800000, v23
	v_med3_f32 v29, v29, s2, v250
	v_add_f32_e32 v30, 1.0, v30
	v_rcp_f32_e32 v30, v30
	s_nop 0
	v_mul_f32_e32 v28, v28, v30
	v_mul_f32_e32 v38, v29, v28
	v_fmamk_f32 v28, v130, 0x3c800000, v6
	v_min_f32_e32 v28, 0x40e00000, v28
	v_mul_f32_e32 v30, 0xc01d265f, v28
	v_exp_f32_e32 v30, v30
	v_fmamk_f32 v29, v98, 0x3c800000, v20
	v_med3_f32 v29, v29, s2, v250
	v_add_f32_e32 v30, 1.0, v30
	v_rcp_f32_e32 v30, v30
	s_nop 0
	v_mul_f32_e32 v28, v28, v30
	v_mul_f32_e32 v39, v29, v28
	v_fmamk_f32 v28, v131, 0x3c800000, v7
	v_min_f32_e32 v28, 0x40e00000, v28
	v_mul_f32_e32 v30, 0xc01d265f, v28
	v_exp_f32_e32 v30, v30
	v_fmamk_f32 v29, v99, 0x3c800000, v21
	v_med3_f32 v29, v29, s2, v250
	v_add_f32_e32 v30, 1.0, v30
	v_rcp_f32_e32 v30, v30
	s_nop 0
	v_mul_f32_e32 v28, v28, v30
	v_mov_b32_e32 v30, v3
	v_cvt_pk_fp8_f32 v30, v31, v34
	v_mov_b32_e32 v31, v3
	v_cvt_pk_fp8_f32 v31, v37, v38
	v_mul_f32_e32 v40, v29, v28
	v_lshl_add_u64 v[28:29], v[24:25], 0, s[0:1]
	v_cvt_pk_fp8_f32 v30, v35, v36 op_sel:[0,0,1]
	v_cvt_pk_fp8_f32 v31, v39, v40 op_sel:[0,0,1]
	s_mov_b64 s[0:1], 0x24000
	global_store_dwordx2 v[28:29], v[30:31], off sc1
	v_fmamk_f32 v28, v124, 0x3c800000, v8
	v_min_f32_e32 v28, 0x40e00000, v28
	v_mul_f32_e32 v30, 0xc01d265f, v28
	v_exp_f32_e32 v30, v30
	v_fmamk_f32 v29, v92, 0x3c800000, v32
	v_med3_f32 v29, v29, s2, v250
	v_add_f32_e32 v30, 1.0, v30
	v_rcp_f32_e32 v30, v30
	s_nop 0
	v_mul_f32_e32 v28, v28, v30
	v_mul_f32_e32 v31, v29, v28
	v_fmamk_f32 v28, v125, 0x3c800000, v9
	v_min_f32_e32 v28, 0x40e00000, v28
	v_mul_f32_e32 v30, 0xc01d265f, v28
	v_exp_f32_e32 v30, v30
	v_fmamk_f32 v29, v93, 0x3c800000, v33
	v_med3_f32 v29, v29, s2, v250
	v_add_f32_e32 v30, 1.0, v30
	v_rcp_f32_e32 v30, v30
	s_nop 0
	v_mul_f32_e32 v28, v28, v30
	v_mul_f32_e32 v34, v29, v28
	v_fmamk_f32 v28, v126, 0x3c800000, v10
	v_min_f32_e32 v28, 0x40e00000, v28
	v_mul_f32_e32 v30, 0xc01d265f, v28
	v_exp_f32_e32 v30, v30
	v_fmamk_f32 v29, v94, 0x3c800000, v26
	v_med3_f32 v29, v29, s2, v250
	v_add_f32_e32 v30, 1.0, v30
	v_rcp_f32_e32 v30, v30
	s_nop 0
	v_mul_f32_e32 v28, v28, v30
	v_mul_f32_e32 v35, v29, v28
	v_fmamk_f32 v28, v127, 0x3c800000, v11
	v_min_f32_e32 v28, 0x40e00000, v28
	v_mul_f32_e32 v30, 0xc01d265f, v28
	v_exp_f32_e32 v30, v30
	v_fmamk_f32 v29, v95, 0x3c800000, v27
	v_med3_f32 v29, v29, s2, v250
	v_add_f32_e32 v30, 1.0, v30
	v_rcp_f32_e32 v30, v30
	s_nop 0
	v_mul_f32_e32 v28, v28, v30
	v_mul_f32_e32 v36, v29, v28
	v_fmamk_f32 v28, v120, 0x3c800000, v4
	v_min_f32_e32 v28, 0x40e00000, v28
	v_mul_f32_e32 v30, 0xc01d265f, v28
	v_exp_f32_e32 v30, v30
	v_fmamk_f32 v29, v88, 0x3c800000, v22
	v_med3_f32 v29, v29, s2, v250
	v_add_f32_e32 v30, 1.0, v30
	v_rcp_f32_e32 v30, v30
	s_nop 0
	v_mul_f32_e32 v28, v28, v30
	v_mul_f32_e32 v37, v29, v28
	v_fmamk_f32 v28, v121, 0x3c800000, v5
	v_min_f32_e32 v28, 0x40e00000, v28
	v_mul_f32_e32 v30, 0xc01d265f, v28
	v_exp_f32_e32 v30, v30
	v_fmamk_f32 v29, v89, 0x3c800000, v23
	v_med3_f32 v29, v29, s2, v250
	v_add_f32_e32 v30, 1.0, v30
	v_rcp_f32_e32 v30, v30
	s_nop 0
	v_mul_f32_e32 v28, v28, v30
	v_mul_f32_e32 v38, v29, v28
	v_fmamk_f32 v28, v122, 0x3c800000, v6
	v_min_f32_e32 v28, 0x40e00000, v28
	v_mul_f32_e32 v30, 0xc01d265f, v28
	v_exp_f32_e32 v30, v30
	v_fmamk_f32 v29, v90, 0x3c800000, v20
	v_med3_f32 v29, v29, s2, v250
	v_add_f32_e32 v30, 1.0, v30
	v_rcp_f32_e32 v30, v30
	s_nop 0
	v_mul_f32_e32 v28, v28, v30
	v_mul_f32_e32 v39, v29, v28
	v_fmamk_f32 v28, v123, 0x3c800000, v7
	v_min_f32_e32 v28, 0x40e00000, v28
	v_mul_f32_e32 v30, 0xc01d265f, v28
	v_exp_f32_e32 v30, v30
	v_fmamk_f32 v29, v91, 0x3c800000, v21
	v_med3_f32 v29, v29, s2, v250
	v_add_f32_e32 v30, 1.0, v30
	v_rcp_f32_e32 v30, v30
	s_nop 0
	v_mul_f32_e32 v28, v28, v30
	v_mov_b32_e32 v30, v3
	v_cvt_pk_fp8_f32 v30, v31, v34
	v_mov_b32_e32 v31, v3
	v_cvt_pk_fp8_f32 v31, v37, v38
	v_mul_f32_e32 v40, v29, v28
	v_lshl_add_u64 v[28:29], v[24:25], 0, s[0:1]
	v_cvt_pk_fp8_f32 v30, v35, v36 op_sel:[0,0,1]
	v_cvt_pk_fp8_f32 v31, v39, v40 op_sel:[0,0,1]
	s_mov_b64 s[0:1], 0x28000
	global_store_dwordx2 v[28:29], v[30:31], off sc1
	v_fmamk_f32 v28, v116, 0x3c800000, v8
	v_min_f32_e32 v28, 0x40e00000, v28
	v_mul_f32_e32 v30, 0xc01d265f, v28
	v_exp_f32_e32 v30, v30
	v_fmamk_f32 v29, v84, 0x3c800000, v32
	v_med3_f32 v29, v29, s2, v250
	v_fmamk_f32 v8, v108, 0x3c800000, v8
	v_add_f32_e32 v30, 1.0, v30
	v_rcp_f32_e32 v30, v30
	v_min_f32_e32 v8, 0x40e00000, v8
	v_mul_f32_e32 v28, v28, v30
	v_mul_f32_e32 v31, v29, v28
	v_fmamk_f32 v28, v117, 0x3c800000, v9
	v_min_f32_e32 v28, 0x40e00000, v28
	v_mul_f32_e32 v30, 0xc01d265f, v28
	v_exp_f32_e32 v30, v30
	v_fmamk_f32 v29, v85, 0x3c800000, v33
	v_med3_f32 v29, v29, s2, v250
	v_fmamk_f32 v9, v109, 0x3c800000, v9
	v_add_f32_e32 v30, 1.0, v30
	v_rcp_f32_e32 v30, v30
	v_min_f32_e32 v9, 0x40e00000, v9
	v_fmac_f32_e32 v33, 0x3c800000, v77
	v_mul_f32_e32 v28, v28, v30
	v_mul_f32_e32 v34, v29, v28
	v_fmamk_f32 v28, v118, 0x3c800000, v10
	v_min_f32_e32 v28, 0x40e00000, v28
	v_mul_f32_e32 v30, 0xc01d265f, v28
	v_exp_f32_e32 v30, v30
	v_fmamk_f32 v29, v86, 0x3c800000, v26
	v_med3_f32 v29, v29, s2, v250
	v_fmamk_f32 v10, v110, 0x3c800000, v10
	v_add_f32_e32 v30, 1.0, v30
	v_rcp_f32_e32 v30, v30
	v_min_f32_e32 v10, 0x40e00000, v10
	v_fmamk_f32 v26, v78, 0x3c800000, v26
	v_med3_f32 v26, v26, s2, v250
	v_mul_f32_e32 v28, v28, v30
	v_mul_f32_e32 v35, v29, v28
	v_fmamk_f32 v28, v119, 0x3c800000, v11
	v_min_f32_e32 v28, 0x40e00000, v28
	v_mul_f32_e32 v30, 0xc01d265f, v28
	v_exp_f32_e32 v30, v30
	v_fmamk_f32 v29, v87, 0x3c800000, v27
	v_med3_f32 v29, v29, s2, v250
	v_fmac_f32_e32 v11, 0x3c800000, v111
	v_add_f32_e32 v30, 1.0, v30
	v_rcp_f32_e32 v30, v30
	v_min_f32_e32 v11, 0x40e00000, v11
	v_fmac_f32_e32 v27, 0x3c800000, v79
	v_mul_f32_e32 v28, v28, v30
	v_mul_f32_e32 v36, v29, v28
	v_fmamk_f32 v28, v112, 0x3c800000, v4
	v_min_f32_e32 v28, 0x40e00000, v28
	v_mul_f32_e32 v30, 0xc01d265f, v28
	v_exp_f32_e32 v30, v30
	v_fmamk_f32 v29, v80, 0x3c800000, v22
	v_med3_f32 v29, v29, s2, v250
	v_fmamk_f32 v4, v104, 0x3c800000, v4
	v_add_f32_e32 v30, 1.0, v30
	v_rcp_f32_e32 v30, v30
	v_min_f32_e32 v4, 0x40e00000, v4
	v_fmamk_f32 v22, v12, 0x3c800000, v22
	v_med3_f32 v22, v22, s2, v250
	v_mul_f32_e32 v28, v28, v30
	v_mul_f32_e32 v37, v29, v28
	v_fmamk_f32 v28, v113, 0x3c800000, v5
	v_min_f32_e32 v28, 0x40e00000, v28
	v_mul_f32_e32 v30, 0xc01d265f, v28
	v_exp_f32_e32 v30, v30
	v_fmamk_f32 v29, v81, 0x3c800000, v23
	v_med3_f32 v29, v29, s2, v250
	v_fmac_f32_e32 v23, 0x3c800000, v13
	v_add_f32_e32 v30, 1.0, v30
	v_rcp_f32_e32 v30, v30
	s_nop 0
	v_mul_f32_e32 v28, v28, v30
	v_mul_f32_e32 v38, v29, v28
	v_fmamk_f32 v28, v114, 0x3c800000, v6
	v_min_f32_e32 v28, 0x40e00000, v28
	v_mul_f32_e32 v30, 0xc01d265f, v28
	v_exp_f32_e32 v30, v30
	v_fmamk_f32 v29, v82, 0x3c800000, v20
	v_med3_f32 v29, v29, s2, v250
	v_add_f32_e32 v30, 1.0, v30
	v_rcp_f32_e32 v30, v30
	s_nop 0
	v_mul_f32_e32 v28, v28, v30
	v_mul_f32_e32 v39, v29, v28
	v_fmamk_f32 v28, v115, 0x3c800000, v7
	v_min_f32_e32 v28, 0x40e00000, v28
	v_mul_f32_e32 v30, 0xc01d265f, v28
	v_exp_f32_e32 v30, v30
	v_fmamk_f32 v29, v83, 0x3c800000, v21
	v_med3_f32 v29, v29, s2, v250
	v_fmac_f32_e32 v7, 0x3c800000, v107
	v_add_f32_e32 v30, 1.0, v30
	v_rcp_f32_e32 v30, v30
	v_fmac_f32_e32 v21, 0x3c800000, v15
	v_mul_f32_e32 v28, v28, v30
	v_mov_b32_e32 v30, v3
	v_cvt_pk_fp8_f32 v30, v31, v34
	v_mov_b32_e32 v31, v3
	v_cvt_pk_fp8_f32 v31, v37, v38
	v_mul_f32_e32 v40, v29, v28
	v_lshl_add_u64 v[28:29], v[24:25], 0, s[0:1]
	v_cvt_pk_fp8_f32 v30, v35, v36 op_sel:[0,0,1]
	v_cvt_pk_fp8_f32 v31, v39, v40 op_sel:[0,0,1]
	s_mov_b64 s[0:1], 0x2c000
	global_store_dwordx2 v[28:29], v[30:31], off sc1
	v_mul_f32_e32 v29, 0xc01d265f, v8
	v_exp_f32_e32 v29, v29
	v_fmamk_f32 v28, v76, 0x3c800000, v32
	v_med3_f32 v28, v28, s2, v250
	v_add_f32_e32 v29, 1.0, v29
	v_rcp_f32_e32 v29, v29
	s_nop 0
	v_mul_f32_e32 v8, v8, v29
	v_mul_f32_e32 v29, 0xc01d265f, v9
	v_exp_f32_e32 v29, v29
	v_mul_f32_e32 v8, v28, v8
	v_med3_f32 v28, v33, s2, v250
	v_add_f32_e32 v29, 1.0, v29
	v_rcp_f32_e32 v29, v29
	s_nop 0
	v_mul_f32_e32 v9, v9, v29
	v_mul_f32_e32 v9, v28, v9
	v_mul_f32_e32 v28, 0xc01d265f, v10
	v_exp_f32_e32 v28, v28
	s_nop 0
	v_add_f32_e32 v28, 1.0, v28
	v_rcp_f32_e32 v28, v28
	s_nop 0
	v_mul_f32_e32 v10, v10, v28
	v_mul_f32_e32 v10, v26, v10
	v_med3_f32 v26, v27, s2, v250
	v_mul_f32_e32 v27, 0xc01d265f, v11
	v_exp_f32_e32 v27, v27
	s_nop 0
	v_add_f32_e32 v27, 1.0, v27
	v_rcp_f32_e32 v27, v27
	s_nop 0
	v_mul_f32_e32 v11, v11, v27
	v_mul_f32_e32 v11, v26, v11
	v_mul_f32_e32 v26, 0xc01d265f, v4
	v_exp_f32_e32 v26, v26
	s_nop 0
	v_add_f32_e32 v26, 1.0, v26
	v_rcp_f32_e32 v26, v26
	s_nop 0
	v_mul_f32_e32 v4, v4, v26
	v_mul_f32_e32 v22, v22, v4
	v_fmamk_f32 v4, v105, 0x3c800000, v5
	v_min_f32_e32 v4, 0x40e00000, v4
	v_med3_f32 v5, v23, s2, v250
	v_mul_f32_e32 v23, 0xc01d265f, v4
	v_exp_f32_e32 v23, v23
	s_nop 0
	v_add_f32_e32 v23, 1.0, v23
	v_rcp_f32_e32 v23, v23
	s_nop 0
	v_mul_f32_e32 v4, v4, v23
	v_mul_f32_e32 v23, v5, v4
	v_fmamk_f32 v4, v106, 0x3c800000, v6
	v_min_f32_e32 v4, 0x40e00000, v4
	v_mul_f32_e32 v6, 0xc01d265f, v4
	v_exp_f32_e32 v6, v6
	v_fmamk_f32 v5, v14, 0x3c800000, v20
	v_med3_f32 v5, v5, s2, v250
	v_add_f32_e32 v6, 1.0, v6
	v_rcp_f32_e32 v6, v6
	s_nop 0
	v_mul_f32_e32 v4, v4, v6
	v_mul_f32_e32 v20, v5, v4
	v_min_f32_e32 v4, 0x40e00000, v7
	v_mul_f32_e32 v6, 0xc01d265f, v4
	v_exp_f32_e32 v6, v6
	v_mov_b32_e32 v7, v3
	v_cvt_pk_fp8_f32 v7, v22, v23
	v_med3_f32 v5, v21, s2, v250
	v_add_f32_e32 v6, 1.0, v6
	v_rcp_f32_e32 v6, v6
	s_nop 0
	v_mul_f32_e32 v4, v4, v6
	v_mov_b32_e32 v6, v3
	v_cvt_pk_fp8_f32 v6, v8, v9
	v_mul_f32_e32 v21, v5, v4
	v_lshl_add_u64 v[4:5], v[24:25], 0, s[0:1]
	v_cvt_pk_fp8_f32 v7, v20, v21 op_sel:[0,0,1]
	v_cvt_pk_fp8_f32 v6, v10, v11 op_sel:[0,0,1]
	s_nop 0
	global_store_dwordx2 v[4:5], v[6:7], off sc1
